# speedup vs baseline: 1.0065x; 1.0065x over previous
.Lh_no_out:
	s_cmp_eq_u32 s17, 0
	s_cselect_b32 s4, s4, s6
	s_cselect_b32 s5, s5, s7
	s_add_u32 s24, s8, s22
	s_addc_u32 s25, s9, 0
	s_add_u32 s4, s4, s21
	s_addc_u32 s5, s5, 0
	global_load_dwordx4 v[14:17], v18, s[24:25] nt
	global_load_dwordx4 v[2:5], v18, s[4:5] nt
	s_add_u32 s6, s4, 0x40000
	s_addc_u32 s7, s5, 0
	s_add_u32 s8, s4, 0x80000
	s_addc_u32 s9, s5, 0
	s_barrier
	global_load_dwordx4 v[6:9], v18, s[6:7] nt
	s_barrier
	global_load_dwordx4 v[10:13], v18, s[8:9] nt
	s_mul_i32 s46, s3, 0xc00
	s_add_u32 s46, s46, 0x8420
	v_lshl_add_u32 v26, v1, 2, s46
	v_and_b32_e32 v38, 15, v0
	s_mul_i32 s58, s17, 0x4200
	s_add_u32 s58, s58, 0x1e0
	v_lshl_add_u32 v38, v38, 2, s58
	v_add_u32_e32 v39, 0x1600, v38
	v_add_u32_e32 v40, 0x2c00, v38
	v_mov_b32_e32 v41, 0x41fc0000
	v_mov_b32_e32 v42, 0xbf38aa3b
	s_mov_b32 s48, 0x3f940000
	s_mov_b32 s51, 0x3fb8aa3b
	s_mov_b32 s42, 0
	s_mov_b32 s43, 0
	s_mov_b32 s44, 0x7fffffff
	s_mov_b32 s45, 0x7fffffff
	s_mov_b32 s47, 0
	s_mul_i32 s58, s3, 0x1600
	s_add_u32 s58, s58, 0x320
	v_lshl_add_u32 v44, v1, 6, s58
	v_bfe_u32 v45, v1, 2, 2
	v_lshlrev_b32_e32 v45, 4, v45
	v_xor_b32_e32 v46, 16, v45
	v_xor_b32_e32 v47, 32, v45
	v_xor_b32_e32 v48, 48, v45
	v_add_u32_e32 v45, v44, v45
	v_add_u32_e32 v46, v44, v46
	v_add_u32_e32 v47, v44, v47
	v_add_u32_e32 v48, v44, v48
	s_mul_i32 s58, s2, 0x600
	s_lshl_b32 s59, s3, 8
	s_add_u32 s58, s58, s59
	s_add_u32 s10, s10, s58
	s_addc_u32 s11, s11, 0
	v_lshlrev_b32_e32 v49, 2, v1
	s_lshl_b32 s58, s2, 2
	s_add_u32 s12, s12, s58
	s_addc_u32 s13, s13, 0
	s_setprio 3
	s_cmp_lt_u32 s3, 8
	s_cbranch_scc1 .Lh_nostagger
	s_sleep 7
